# P6 epilogue staging by LDS-DMA (24 global_load_lds, one exposed round trip instead of two)
# baseline (speedup 1.0000x reference)
.LBB0_975:
	s_add_i32 s0, s96, s35
	s_ashr_i32 s1, s0, 31
	s_lshr_b32 s1, s1, 19
	s_add_i32 s0, s0, s1
	s_ashr_i32 s2, s0, 13
	s_xor_b64 s[14:15], s[6:7], -1
	s_ashr_i32 s0, s2, 31
	s_add_u32 s1, s2, s87
	s_addc_u32 s0, s0, 0
	s_waitcnt vmcnt(0)
	v_lshlrev_b32_e32 v186, 6, v179
	v_lshl_add_u32 v185, v179, 4, s85
	v_mov_b32_e32 v187, 0
	s_mul_i32 s40, s1, 0x6000
	s_add_u32 s40, s70, s40
	s_addc_u32 s41, s71, 0
	s_add_u32 s42, s40, 0x5000
	s_addc_u32 s43, s41, 0
	s_add_u32 s40, s40, 0x18000
	s_addc_u32 s41, s41, 0
	v_mov_b32_e32 v188, 0x10000
	v_lshl_add_u32 v188, v179, 4, v188
	s_add_i32 m0, s85, 0
	s_nop 0
	global_load_lds_dwordx4 v186, s[16:17] offset:0
	s_add_i32 m0, s85, 1008
	s_nop 0
	global_load_lds_dwordx4 v186, s[16:17] offset:16
	s_add_i32 m0, s85, 2016
	s_nop 0
	global_load_lds_dwordx4 v186, s[16:17] offset:32
	s_add_i32 m0, s85, 3024
	s_nop 0
	global_load_lds_dwordx4 v186, s[16:17] offset:48
	s_add_i32 m0, s85, 4096
	s_nop 0
	global_load_lds_dwordx4 v186, s[28:29] offset:0
	s_add_i32 m0, s85, 5104
	s_nop 0
	global_load_lds_dwordx4 v186, s[28:29] offset:16
	s_add_i32 m0, s85, 6112
	s_nop 0
	global_load_lds_dwordx4 v186, s[28:29] offset:32
	s_add_i32 m0, s85, 7120
	s_nop 0
	global_load_lds_dwordx4 v186, s[28:29] offset:48
	s_add_i32 m0, s85, 8192
	s_nop 0
	global_load_lds_dwordx4 v186, s[12:13] offset:0
	s_add_i32 m0, s85, 9200
	s_nop 0
	global_load_lds_dwordx4 v186, s[12:13] offset:16
	s_add_i32 m0, s85, 10208
	s_nop 0
	global_load_lds_dwordx4 v186, s[12:13] offset:32
	s_add_i32 m0, s85, 11216
	s_nop 0
	global_load_lds_dwordx4 v186, s[12:13] offset:48
	s_add_i32 m0, s85, 12288
	s_nop 0
	global_load_lds_dwordx4 v186, s[90:91] offset:0
	s_add_i32 m0, s85, 13296
	s_nop 0
	global_load_lds_dwordx4 v186, s[90:91] offset:16
	s_add_i32 m0, s85, 14304
	s_nop 0
	global_load_lds_dwordx4 v186, s[90:91] offset:32
	s_add_i32 m0, s85, 15312
	s_nop 0
	global_load_lds_dwordx4 v186, s[90:91] offset:48
	s_mov_b32 m0, 65536
	s_nop 0
	global_load_lds_dwordx4 v186, s[42:43] offset:0
	s_mov_b32 m0, 66544
	s_nop 0
	global_load_lds_dwordx4 v186, s[42:43] offset:16
	s_mov_b32 m0, 67552
	s_nop 0
	global_load_lds_dwordx4 v186, s[42:43] offset:32
	s_mov_b32 m0, 68560
	s_nop 0
	global_load_lds_dwordx4 v186, s[42:43] offset:48
	s_mov_b32 m0, 69632
	s_nop 0
	global_load_lds_dwordx4 v186, s[40:41] offset:0
	s_mov_b32 m0, 70640
	s_nop 0
	global_load_lds_dwordx4 v186, s[40:41] offset:16
	s_mov_b32 m0, 71648
	s_nop 0
	global_load_lds_dwordx4 v186, s[40:41] offset:32
	s_mov_b32 m0, 72656
	s_nop 0
	global_load_lds_dwordx4 v186, s[40:41] offset:48
	v_readlane_b32 s40, v253, 62
	v_readlane_b32 s41, v253, 63
	s_lshl_b64 s[44:45], s[96:97], 12
	v_lshlrev_b32_e32 v2, 6, v179
	s_add_u32 s40, s40, s44
	s_addc_u32 s41, s41, s45
	s_add_u32 s40, s40, 0x1000
	s_addc_u32 s41, s41, 0
	global_load_dword v184, v2, s[40:41]
	s_add_u32 s40, s40, 0x1000
	s_addc_u32 s41, s41, 0
	global_load_dword v184, v2, s[40:41]
	s_add_u32 s40, s40, 0x1000
	s_addc_u32 s41, s41, 0
	global_load_dword v184, v2, s[40:41]
	s_waitcnt vmcnt(3)
	v_mov_b32_e32 v1, v179
	s_mulk_i32 s0, 0x6000
	s_mul_hi_u32 s3, s1, 0x6000
	s_add_i32 s3, s3, s0
	s_mulk_i32 s1, 0x6000
	v_lshlrev_b32_e32 v20, 4, v1
	s_add_u32 s6, s70, s1
	v_readlane_b32 s36, v253, 60
	v_ashrrev_i32_e32 v21, 31, v20
	s_addc_u32 s7, s71, s3
	s_lshl_b64 s[0:1], s[96:97], 12
	v_readlane_b32 s38, v253, 62
	v_lshlrev_b64 v[22:23], 2, v[20:21]
	v_readlane_b32 s39, v253, 63
	s_add_u32 s20, s38, s0
	v_lshl_add_u64 v[68:69], s[6:7], 0, v[22:23]
	s_mov_b64 s[6:7], 0x5000
	s_addc_u32 s21, s39, s1
	v_lshl_add_u64 v[12:13], v[68:69], 0, s[6:7]
	s_lshl_b64 s[6:7], s[96:97], 3
	v_lshl_add_u64 v[32:33], s[20:21], 0, v[22:23]
	s_add_u32 s6, s64, s6
	ds_read_b128 v[4:7], v188 offset:3072
	ds_read_b128 v[8:11], v188 offset:2048
	s_addc_u32 s7, s65, s7
	ds_read_b128 v[12:15], v188 offset:1024
	s_nop 0
	global_load_dwordx2 v[72:73], v3, s[6:7]
	global_load_dwordx4 v[16:19], v[32:33], off
	global_load_dwordx4 v[24:27], v[32:33], off offset:16
	global_load_dwordx4 v[28:31], v[32:33], off offset:32
	s_nop 0
	global_load_dwordx4 v[32:35], v[32:33], off offset:48
	v_lshl_add_u64 v[60:61], s[16:17], 0, v[22:23]
	v_lshl_add_u64 v[64:65], s[28:29], 0, v[22:23]
	v_add_co_u32_e32 v68, vcc, s18, v68
	ds_read_b128 v[36:39], v185 offset:7168
	ds_read_b128 v[40:43], v185 offset:3072
	ds_read_b128 v[44:47], v185 offset:2048
	ds_read_b128 v[48:51], v185 offset:6144
	ds_read_b128 v[52:55], v185 offset:5120
	ds_read_b128 v[56:59], v185 offset:1024
	s_nop 0
	ds_read_b128 v[60:63], v185 offset:0
	s_nop 0
	ds_read_b128 v[64:67], v185 offset:4096
	v_addc_co_u32_e32 v69, vcc, 0, v69, vcc
	ds_read_b128 v[68:71], v188 offset:0
	v_add_u32_e32 v142, 64, v183
	v_xor_b32_e32 v1, 1, v178
	v_xor_b32_e32 v2, 2, v178
	v_cmp_lt_i32_e32 vcc, v1, v142
	v_xor_b32_e32 v74, 4, v178
	v_readlane_b32 s20, v255, 42
	v_cndmask_b32_e32 v1, v178, v1, vcc
	v_cmp_lt_i32_e32 vcc, v2, v142
	v_readlane_b32 s22, v255, 44
	s_add_u32 s0, s30, s0
	v_cndmask_b32_e32 v75, v178, v2, vcc
	v_lshlrev_b32_e32 v2, 2, v1
	v_lshlrev_b32_e32 v1, 2, v75
	v_cmp_lt_i32_e32 vcc, v74, v142
	s_addc_u32 s1, s31, s1
	v_readlane_b32 s37, v253, 61
	v_readlane_b32 s40, v254, 0
	v_readlane_b32 s41, v254, 1
	v_readlane_b32 s42, v254, 2
	v_readlane_b32 s43, v254, 3
	v_readlane_b32 s44, v254, 4
	v_readlane_b32 s45, v254, 5
	v_readlane_b32 s46, v254, 6
	v_readlane_b32 s47, v254, 7
	v_readlane_b32 s48, v254, 8
	v_readlane_b32 s49, v254, 9
	v_readlane_b32 s50, v254, 10
	v_readlane_b32 s51, v254, 11
	v_readlane_b32 s21, v255, 43
	v_readlane_b32 s23, v255, 45
	s_waitcnt lgkmcnt(0)
	s_waitcnt vmcnt(5)
	v_pk_add_f32 v[12:13], v[12:13], 1.0 op_sel_hi:[1,0]
	v_pk_add_f32 v[14:15], v[14:15], 1.0 op_sel_hi:[1,0]
	s_waitcnt lgkmcnt(0)
	s_waitcnt vmcnt(3)
	v_pk_add_f32 v[18:19], v[18:19], v[72:73] op_sel_hi:[1,0] neg_lo:[0,1] neg_hi:[0,1]
	v_pk_add_f32 v[4:5], v[4:5], 1.0 op_sel_hi:[1,0]
	v_pk_mul_f32 v[18:19], v[72:73], v[18:19] op_sel:[1,0]
	s_waitcnt lgkmcnt(0)
	s_waitcnt vmcnt(0)
	v_pk_add_f32 v[32:33], v[32:33], v[72:73] op_sel_hi:[1,0] neg_lo:[0,1] neg_hi:[0,1]
	v_pk_add_f32 v[34:35], v[34:35], v[72:73] op_sel_hi:[1,0] neg_lo:[0,1] neg_hi:[0,1]
	v_pk_mul_f32 v[32:33], v[72:73], v[32:33] op_sel:[1,0]
	v_pk_mul_f32 v[34:35], v[72:73], v[34:35] op_sel:[1,0]
	s_waitcnt lgkmcnt(0)
	s_waitcnt vmcnt(0)
	v_pk_fma_f32 v[32:33], v[32:33], v[40:41], v[36:37]
	v_pk_fma_f32 v[34:35], v[34:35], v[42:43], v[38:39]
	v_pk_mul_f32 v[32:33], v[32:33], s[34:35] op_sel_hi:[1,0]
	v_pk_add_f32 v[6:7], v[6:7], 1.0 op_sel_hi:[1,0]
	v_pk_add_f32 v[24:25], v[24:25], v[72:73] op_sel_hi:[1,0] neg_lo:[0,1] neg_hi:[0,1]
	v_pk_mul_f32 v[34:35], v[34:35], s[34:35] op_sel_hi:[1,0]
	v_pk_fma_f32 v[42:43], v[138:139], v[4:5], v[32:33]
	s_waitcnt lgkmcnt(0)
	s_waitcnt vmcnt(0)
	v_pk_fma_f32 v[4:5], v[18:19], v[62:63], v[66:67]
	v_pk_add_f32 v[16:17], v[16:17], v[72:73] op_sel_hi:[1,0] neg_lo:[0,1] neg_hi:[0,1]
	v_pk_mul_f32 v[24:25], v[72:73], v[24:25] op_sel:[1,0]
	v_pk_fma_f32 v[40:41], v[140:141], v[6:7], v[34:35]
	v_pk_mul_f32 v[4:5], v[4:5], s[34:35] op_sel_hi:[1,0]
	s_waitcnt lgkmcnt(0)
	s_waitcnt vmcnt(0)
	v_pk_add_f32 v[6:7], v[70:71], 1.0 op_sel_hi:[1,0]
	v_pk_fma_f32 v[24:25], v[24:25], v[56:57], v[52:53]
	v_pk_fma_f32 v[52:53], v[128:129], v[6:7], v[4:5]
	v_pk_mul_f32 v[4:5], v[72:73], v[16:17] op_sel:[1,0]
	v_pk_add_f32 v[26:27], v[26:27], v[72:73] op_sel_hi:[1,0] neg_lo:[0,1] neg_hi:[0,1]
	v_pk_fma_f32 v[4:5], v[60:61], v[4:5], v[64:65]
	v_pk_mul_f32 v[26:27], v[72:73], v[26:27] op_sel:[1,0]
	v_pk_mul_f32 v[4:5], v[4:5], s[34:35] op_sel_hi:[1,0]
	v_pk_add_f32 v[6:7], v[68:69], 1.0 op_sel_hi:[1,0]
	v_pk_fma_f32 v[26:27], v[26:27], v[58:59], v[54:55]
	v_pk_fma_f32 v[54:55], v[126:127], v[6:7], v[4:5]
	v_pk_add_f32 v[30:31], v[30:31], v[72:73] op_sel_hi:[1,0] neg_lo:[0,1] neg_hi:[0,1]
	v_add_f32_e32 v4, 0, v54
	v_add_f32_e32 v4, v4, v55
	v_pk_mul_f32 v[30:31], v[72:73], v[30:31] op_sel:[1,0]
	v_pk_mul_f32 v[24:25], v[24:25], s[34:35] op_sel_hi:[1,0]
	v_add_f32_e32 v4, v4, v52
	v_pk_add_f32 v[28:29], v[28:29], v[72:73] op_sel_hi:[1,0] neg_lo:[0,1] neg_hi:[0,1]
	v_pk_fma_f32 v[30:31], v[30:31], v[46:47], v[50:51]
	v_pk_fma_f32 v[50:51], v[130:131], v[12:13], v[24:25]
	v_add_f32_e32 v4, v4, v53
	v_pk_mul_f32 v[28:29], v[72:73], v[28:29] op_sel:[1,0]
	v_pk_mul_f32 v[26:27], v[26:27], s[34:35] op_sel_hi:[1,0]
	v_add_f32_e32 v4, v4, v50
	v_pk_fma_f32 v[28:29], v[28:29], v[44:45], v[48:49]
	v_pk_fma_f32 v[48:49], v[132:133], v[14:15], v[26:27]
	v_add_f32_e32 v4, v4, v51
	v_pk_add_f32 v[8:9], v[8:9], 1.0 op_sel_hi:[1,0]
	v_pk_mul_f32 v[28:29], v[28:29], s[34:35] op_sel_hi:[1,0]
	v_add_f32_e32 v4, v4, v48
	v_pk_fma_f32 v[46:47], v[134:135], v[8:9], v[28:29]
	v_add_f32_e32 v4, v4, v49
	v_pk_add_f32 v[10:11], v[10:11], 1.0 op_sel_hi:[1,0]
	v_pk_mul_f32 v[30:31], v[30:31], s[34:35] op_sel_hi:[1,0]
	v_add_f32_e32 v4, v4, v46
	v_pk_fma_f32 v[44:45], v[136:137], v[10:11], v[30:31]
	v_add_f32_e32 v4, v4, v47
	v_add_f32_e32 v4, v4, v44
	v_add_f32_e32 v4, v4, v45
	v_add_f32_e32 v4, v4, v42
	v_add_f32_e32 v4, v4, v43
	v_add_f32_e32 v4, v4, v40
	v_add_f32_e32 v4, v4, v41
	ds_bpermute_b32 v5, v2, v4
	v_cndmask_b32_e32 v6, v178, v74, vcc
	v_lshlrev_b32_e32 v74, 2, v6
	v_xor_b32_e32 v6, 8, v178
	v_cmp_lt_i32_e32 vcc, v6, v142
	s_waitcnt lgkmcnt(0)
	v_add_f32_e32 v4, v4, v5
	ds_bpermute_b32 v5, v1, v4
	v_cndmask_b32_e32 v6, v178, v6, vcc
	v_lshlrev_b32_e32 v75, 2, v6
	v_xor_b32_e32 v6, 16, v178
	v_cmp_lt_i32_e32 vcc, v6, v142
	s_waitcnt lgkmcnt(0)
	v_add_f32_e32 v4, v4, v5
	ds_bpermute_b32 v5, v74, v4
	v_cndmask_b32_e32 v6, v178, v6, vcc
	v_lshlrev_b32_e32 v126, 2, v6
	v_xor_b32_e32 v6, 32, v178
	v_cmp_lt_i32_e32 vcc, v6, v142
	s_waitcnt lgkmcnt(0)
	v_add_f32_e32 v7, v4, v5
	ds_bpermute_b32 v8, v75, v7
	v_cndmask_b32_e32 v4, v178, v6, vcc
	v_lshlrev_b32_e32 v127, 2, v4
	v_lshl_add_u64 v[4:5], s[12:13], 0, v[22:23]
	v_lshl_add_u64 v[36:37], s[90:91], 0, v[22:23]
	s_waitcnt lgkmcnt(0)
	v_add_f32_e32 v24, v7, v8
	ds_bpermute_b32 v25, v126, v24
	ds_read_b128 v[16:19], v185 offset:11264
	ds_read_b128 v[12:15], v185 offset:10240
	ds_read_b128 v[8:11], v185 offset:9216
	s_nop 0
	ds_read_b128 v[4:7], v185 offset:8192
	v_lshl_add_u64 v[22:23], s[0:1], 0, v[22:23]
	v_readlane_b32 s0, v255, 23
	v_readlane_b32 s1, v255, 24
	s_waitcnt lgkmcnt(0)
	v_add_f32_e32 v56, v24, v25
	ds_read_b128 v[24:27], v185 offset:15360
	ds_read_b128 v[28:31], v185 offset:14336
	ds_read_b128 v[32:35], v185 offset:13312
	s_nop 0
	ds_read_b128 v[36:39], v185 offset:12288
	ds_bpermute_b32 v57, v127, v56
	s_waitcnt lgkmcnt(0)
	v_add_f32_e32 v56, v56, v57
	v_mul_f32_e32 v56, 0x3a800000, v56
	v_pk_add_f32 v[54:55], v[54:55], v[56:57] op_sel_hi:[1,0] neg_lo:[0,1] neg_hi:[0,1]
	v_pk_add_f32 v[52:53], v[52:53], v[56:57] op_sel_hi:[1,0] neg_lo:[0,1] neg_hi:[0,1]
	v_pk_mul_f32 v[58:59], v[54:55], v[54:55]
	v_pk_mul_f32 v[60:61], v[52:53], v[52:53]
	v_add_f32_e32 v58, v58, v59
	v_pk_add_f32 v[50:51], v[50:51], v[56:57] op_sel_hi:[1,0] neg_lo:[0,1] neg_hi:[0,1]
	v_add_f32_e32 v58, v60, v58
	v_pk_mul_f32 v[62:63], v[50:51], v[50:51]
	v_add_f32_e32 v58, v61, v58
	v_pk_add_f32 v[48:49], v[48:49], v[56:57] op_sel_hi:[1,0] neg_lo:[0,1] neg_hi:[0,1]
	v_add_f32_e32 v58, v62, v58
	v_pk_mul_f32 v[64:65], v[48:49], v[48:49]
	v_add_f32_e32 v58, v63, v58
	v_pk_add_f32 v[46:47], v[46:47], v[56:57] op_sel_hi:[1,0] neg_lo:[0,1] neg_hi:[0,1]
	v_add_f32_e32 v58, v64, v58
	v_pk_mul_f32 v[66:67], v[46:47], v[46:47]
	v_add_f32_e32 v58, v65, v58
	v_pk_add_f32 v[44:45], v[44:45], v[56:57] op_sel_hi:[1,0] neg_lo:[0,1] neg_hi:[0,1]
	v_add_f32_e32 v58, v66, v58
	v_pk_mul_f32 v[68:69], v[44:45], v[44:45]
	v_add_f32_e32 v58, v67, v58
	v_pk_add_f32 v[42:43], v[42:43], v[56:57] op_sel_hi:[1,0] neg_lo:[0,1] neg_hi:[0,1]
	v_add_f32_e32 v58, v68, v58
	v_pk_mul_f32 v[70:71], v[42:43], v[42:43]
	v_add_f32_e32 v58, v69, v58
	v_pk_add_f32 v[40:41], v[40:41], v[56:57] op_sel_hi:[1,0] neg_lo:[0,1] neg_hi:[0,1]
	v_add_f32_e32 v58, v70, v58
	v_pk_mul_f32 v[56:57], v[40:41], v[40:41]
	v_add_f32_e32 v58, v71, v58
	v_add_f32_e32 v56, v56, v58
	v_add_f32_e32 v56, v57, v56
	ds_bpermute_b32 v57, v2, v56
	s_waitcnt lgkmcnt(0)
	v_add_f32_e32 v56, v56, v57
	ds_bpermute_b32 v57, v1, v56
	s_waitcnt lgkmcnt(0)
	v_add_f32_e32 v56, v56, v57
	ds_bpermute_b32 v57, v74, v56
	s_waitcnt lgkmcnt(0)
	v_add_f32_e32 v56, v56, v57
	ds_bpermute_b32 v57, v75, v56
	s_waitcnt lgkmcnt(0)
	v_add_f32_e32 v56, v56, v57
	ds_bpermute_b32 v57, v126, v56
	s_waitcnt lgkmcnt(0)
	v_add_f32_e32 v56, v56, v57
	ds_bpermute_b32 v57, v127, v56
	s_waitcnt lgkmcnt(0)
	v_add_f32_e32 v56, v56, v57
	v_fmamk_f32 v56, v56, 0x3a800000, v204
	v_mul_f32_e32 v57, 0x4b800000, v56
	v_cmp_gt_f32_e32 vcc, s22, v56
	s_nop 1
	v_cndmask_b32_e32 v56, v56, v57, vcc
	v_rsq_f32_e32 v56, v56
	s_nop 0
	v_mul_f32_e32 v57, 0x45800000, v56
	v_cndmask_b32_e32 v56, v56, v57, vcc
	v_pk_mul_f32 v[54:55], v[54:55], v[56:57] op_sel_hi:[1,0]
	v_pk_mul_f32 v[52:53], v[52:53], v[56:57] op_sel_hi:[1,0]
	s_waitcnt lgkmcnt(0)
	s_waitcnt vmcnt(0)
	v_pk_fma_f32 v[4:5], v[4:5], v[54:55], v[36:37]
	v_pk_mul_f32 v[36:37], v[50:51], v[56:57] op_sel_hi:[1,0]
	v_pk_fma_f32 v[6:7], v[6:7], v[52:53], v[38:39]
	v_pk_fma_f32 v[8:9], v[8:9], v[36:37], v[32:33]
	v_pk_mul_f32 v[32:33], v[48:49], v[56:57] op_sel_hi:[1,0]
	s_and_b64 vcc, exec, s[0:1]
	v_pk_fma_f32 v[10:11], v[10:11], v[32:33], v[34:35]
	v_pk_mul_f32 v[32:33], v[46:47], v[56:57] op_sel_hi:[1,0]
	s_nop 0
	v_pk_fma_f32 v[12:13], v[12:13], v[32:33], v[28:29]
	v_pk_mul_f32 v[28:29], v[44:45], v[56:57] op_sel_hi:[1,0]
	s_nop 0
	v_pk_fma_f32 v[14:15], v[14:15], v[28:29], v[30:31]
	v_pk_mul_f32 v[28:29], v[42:43], v[56:57] op_sel_hi:[1,0]
	s_nop 0
	v_pk_fma_f32 v[16:17], v[16:17], v[28:29], v[24:25]
	v_pk_mul_f32 v[24:25], v[40:41], v[56:57] op_sel_hi:[1,0]
	s_nop 0
	v_pk_fma_f32 v[18:19], v[18:19], v[24:25], v[26:27]
	global_store_dwordx4 v[22:23], v[4:7], off
	global_store_dwordx4 v[22:23], v[8:11], off offset:16
	global_store_dwordx4 v[22:23], v[12:15], off offset:32
	global_store_dwordx4 v[22:23], v[16:19], off offset:48
	s_cbranch_vccz .LBB0_977
	s_lshl_b64 s[0:1], s[96:97], 10
	s_mul_hi_i32 s3, s2, 0x6000
	s_mulk_i32 s2, 0x6000
	s_add_u32 s2, s70, s2
	s_addc_u32 s3, s71, s3
	v_lshl_add_u64 v[50:51], v[20:21], 2, s[2:3]
	s_mov_b64 s[2:3], 0x19000
	v_add_co_u32_e32 v34, vcc, s86, v50
	v_lshl_add_u64 v[30:31], v[50:51], 0, s[2:3]
	s_mov_b64 s[2:3], 0x18000
	v_addc_co_u32_e32 v35, vcc, 0, v51, vcc
	v_lshl_add_u64 v[46:47], v[50:51], 0, s[2:3]
	v_add_co_u32_e32 v50, vcc, s67, v50
	global_load_dwordx4 v[22:25], v[30:31], off offset:32
	global_load_dwordx4 v[26:29], v[30:31], off offset:16
	v_addc_co_u32_e32 v51, vcc, 0, v51, vcc
	global_load_dwordx4 v[30:33], v[30:31], off offset:48
	s_nop 0
	global_load_dwordx4 v[34:37], v[34:35], off
	s_nop 0
	ds_read_b128 v[38:41], v188 offset:5120
	ds_read_b128 v[42:45], v188 offset:7168
	s_nop 0
	ds_read_b128 v[46:49], v188 offset:6144
	s_lshl_b64 s[0:1], s[0:1], 1
	ds_read_b128 v[50:53], v188 offset:4096
	s_add_u32 s0, s76, s0
	s_addc_u32 s1, s77, s1
	v_lshl_add_u64 v[20:21], v[20:21], 1, s[0:1]
	s_waitcnt lgkmcnt(0)
	s_waitcnt vmcnt(3)
	v_pk_add_f32 v[22:23], v[22:23], 1.0 op_sel_hi:[1,0]
	s_waitcnt lgkmcnt(0)
	s_waitcnt vmcnt(2)
	v_pk_add_f32 v[26:27], v[26:27], 1.0 op_sel_hi:[1,0]
	v_pk_add_f32 v[28:29], v[28:29], 1.0 op_sel_hi:[1,0]
	s_waitcnt lgkmcnt(0)
	s_waitcnt vmcnt(0)
	v_pk_add_f32 v[34:35], v[34:35], 1.0 op_sel_hi:[1,0]
	v_pk_add_f32 v[36:37], v[36:37], 1.0 op_sel_hi:[1,0]
	v_pk_add_f32 v[24:25], v[24:25], 1.0 op_sel_hi:[1,0]
	v_pk_add_f32 v[30:31], v[30:31], 1.0 op_sel_hi:[1,0]
	v_pk_add_f32 v[32:33], v[32:33], 1.0 op_sel_hi:[1,0]
	s_waitcnt lgkmcnt(0)
	s_waitcnt vmcnt(0)
	v_pk_fma_f32 v[8:9], v[8:9], v[26:27], v[38:39]
	v_pk_fma_f32 v[10:11], v[10:11], v[28:29], v[40:41]
	s_waitcnt lgkmcnt(0)
	s_waitcnt vmcnt(0)
	v_pk_fma_f32 v[12:13], v[12:13], v[22:23], v[46:47]
	s_waitcnt lgkmcnt(0)
	s_waitcnt vmcnt(0)
	v_pk_fma_f32 v[4:5], v[4:5], v[34:35], v[50:51]
	v_pk_fma_f32 v[22:23], v[6:7], v[36:37], v[52:53]
	v_pk_fma_f32 v[14:15], v[14:15], v[24:25], v[48:49]
	v_pk_fma_f32 v[16:17], v[16:17], v[30:31], v[42:43]
	v_pk_fma_f32 v[18:19], v[18:19], v[32:33], v[44:45]
	v_cvt_pk_bf16_f32 v6, v8, v9
	v_cvt_pk_bf16_f32 v7, v10, v11
	v_cvt_pk_bf16_f32 v4, v4, v5
	v_cvt_pk_bf16_f32 v5, v22, v23
	v_cvt_pk_bf16_f32 v8, v12, v13
	v_cvt_pk_bf16_f32 v9, v14, v15
	v_cvt_pk_bf16_f32 v10, v16, v17
	v_cvt_pk_bf16_f32 v11, v18, v19
	global_store_dwordx4 v[20:21], v[4:7], off
	global_store_dwordx4 v[20:21], v[8:11], off offset:16
